# q3 with the compiler's original lgkmcnt waits (20 fewer s_waitcnt per iteration)
# baseline (speedup 1.0000x reference)
; template <bool FIRST> DEVI bool partialSM(f32x16& p0, f32x16& p1, float& m_reg, float& alpha) {
;     float pmax = p0[0];
; #pragma unroll
;     for (int r = 1; r < 16; ++r) pmax = fmaxf(pmax, p0[r]);
; #pragma unroll
;     for (int r = 0; r < 16; ++r) pmax = fmaxf(pmax, p1[r]);
;     { auto rr = __builtin_amdgcn_permlane32_swap(__float_as_uint(pmax), __float_as_uint(pmax), false, false);
;       pmax = fmaxf(__uint_as_float(rr[0]), __uint_as_float(rr[1])); }
;     if (FIRST) { m_reg = pmax; alpha = 1.f;
; #pragma unroll
;         for (int r = 0; r < 16; ++r) { p0[r] = __builtin_amdgcn_exp2f(p0[r] - pmax); p1[r] = p1[r] - pmax; }
;         return false;
;     } else if (__builtin_expect(__all(pmax <= ATT_THR), 1)) { alpha = 1.f;
; #pragma unroll
;         for (int r = 0; r < 16; ++r) p0[r] = __builtin_amdgcn_exp2f(p0[r]);
;         return false;
;     } else { const float d = fmaxf(pmax, 0.f); alpha = __builtin_amdgcn_exp2f(-d); m_reg += d;
; #pragma unroll
;         for (int r = 0; r < 16; ++r) { p0[r] = __builtin_amdgcn_exp2f(p0[r] - d); p1[r] = p1[r] - d; }
;         return true;
;     }
; }
; DEVI void finishSM(f32x16& p0, f32x16& p1, float alpha, float& l_reg, bf16x8& pa0, bf16x8& pa1, bf16x8& pa2, bf16x8& pa3) {
; #pragma unroll
;     for (int r = 0; r < 16; ++r) p1[r] = __builtin_amdgcn_exp2f(p1[r]);
;     f32x2 s2 = (f32x2){p0[0], p0[1]} + (f32x2){p1[0], p1[1]};
; #pragma unroll
;     for (int r = 2; r < 16; r += 2) s2 += (f32x2){p0[r], p0[r + 1]} + (f32x2){p1[r], p1[r + 1]};
;     float ps = s2[0] + s2[1];
;     { auto rr = __builtin_amdgcn_permlane32_swap(__float_as_uint(ps), __float_as_uint(ps), false, false);
;       ps = __uint_as_float(rr[0]) + __uint_as_float(rr[1]); }
;     l_reg = l_reg * alpha + ps;
;     ...
;     PK4(p0, 0, pa0); PK4(p0, 8, pa1); PK4(p1, 0, pa2); PK4(p1, 8, pa3);
;     ...
; }
; DEVI void qkt(f32x16& p0, f32x16& p1, const char* Kb, const bf16x8 (&qr)[6], int r32, int hi, const f32x16& cinit) {
; #pragma unroll
;     for (int d0 = 0; d0 < 6; ++d0) { const int cb = (d0 * 16 + hi * 8) * 2;
;         const bf16x8 k0 = *(const bf16x8*)(Kb + KSWZ(r32, cb)), k1 = *(const bf16x8*)(Kb + KSWZ(32 + r32, cb));
;         p0 = __builtin_amdgcn_mfma_f32_32x32x16_bf16(k0, qr[d0], d0 == 0 ? cinit : p0, 0, 0, 0);
;         p1 = __builtin_amdgcn_mfma_f32_32x32x16_bf16(k1, qr[d0], d0 == 0 ? cinit : p1, 0, 0, 0); }
; }
.LBB0_696:
	v_add_u32_e32 v174, s98, v204
	v_exp_f32_e32 v66, v66
	v_exp_f32_e32 v67, v67
	s_waitcnt lgkmcnt(0)
	v_mfma_f32_32x32x16_bf16 v[98:113], v[82:85], v[150:153], v[34:49]
	v_add_u32_e32 v82, s98, v184
	v_add_u32_e32 v83, s98, v185
	ds_read_b128 v[208:211], v82 offset:12288
	ds_read_b128 v[212:215], v82 offset:18432
	ds_read_b128 v[216:219], v83 offset:12288
	ds_read_b128 v[220:223], v83 offset:18432
	v_exp_f32_e32 v68, v68
	v_exp_f32_e32 v69, v69
	v_exp_f32_e32 v70, v70
	v_exp_f32_e32 v71, v71
	s_waitcnt lgkmcnt(4)
	v_mfma_f32_32x32x16_bf16 v[82:97], v[124:127], v[150:153], v[34:49]
	ds_read_b128 v[124:127], v174 offset:12288
	ds_read_b128 v[224:227], v174 offset:18432
	v_exp_f32_e32 v72, v72
	v_exp_f32_e32 v73, v73
	v_exp_f32_e32 v74, v74
	v_exp_f32_e32 v75, v75
	v_exp_f32_e32 v76, v76
	v_exp_f32_e32 v77, v77
	s_waitcnt lgkmcnt(0)
	v_mfma_f32_32x32x16_bf16 v[98:113], v[208:211], v[138:141], v[98:113]
	v_add_u32_e32 v174, s98, v205
	v_exp_f32_e32 v78, v78
	v_exp_f32_e32 v79, v79
	ds_read_b128 v[228:231], v174 offset:12288
	ds_read_b128 v[232:235], v174 offset:18432
	v_exp_f32_e32 v80, v80
	v_exp_f32_e32 v81, v81
	v_add_u32_e32 v174, s98, v206
	s_waitcnt lgkmcnt(6)
	v_mfma_f32_32x32x16_bf16 v[82:97], v[212:215], v[138:141], v[82:97]
	v_add_f32_e64 v212, v50, v66
	v_add_f32_e64 v213, v51, v67
	v_add_f32_e64 v214, v52, v68
	v_add_f32_e64 v215, v53, v69
	v_lshl_add_u32 v202, s89, 14, v115
	v_add_f32_e32 v212, v214, v212
	v_add_f32_e32 v213, v215, v213
	v_add_f32_e32 v214, v54, v70
	v_add_f32_e32 v215, v55, v71
	ds_read_b128 v[208:211], v174 offset:12288
	ds_read_b128 v[236:239], v174 offset:18432
	v_add_f32_e32 v212, v214, v212
	v_add_f32_e32 v213, v215, v213
	s_waitcnt lgkmcnt(7)
	v_mfma_f32_32x32x16_bf16 v[98:113], v[216:219], v[134:137], v[98:113]
	v_add_f32_e64 v214, v56, v72
	v_add_f32_e64 v215, v57, v73
	v_cvt_pk_bf16_f32 v50, v50, v51
	v_cvt_pk_bf16_f32 v51, v52, v53
	v_cvt_pk_bf16_f32 v52, v54, v55
	v_cvt_pk_bf16_f32 v53, v56, v57
	v_cvt_pk_bf16_f32 v54, v58, v59
	v_add_f32_e64 v212, v214, v212
	v_add_f32_e64 v213, v215, v213
	s_waitcnt lgkmcnt(6)
	v_mfma_f32_32x32x16_bf16 v[82:97], v[220:223], v[134:137], v[82:97]
	v_add_f32_e64 v214, v58, v74
	v_add_f32_e64 v215, v59, v75
	v_cvt_pk_bf16_f32 v55, v60, v61
	v_cvt_pk_bf16_f32 v56, v62, v63
	v_cvt_pk_bf16_f32 v57, v64, v65
	v_cvt_pk_bf16_f32 v58, v66, v67
	v_cvt_pk_bf16_f32 v59, v68, v69
	v_add_f32_e64 v212, v214, v212
	v_add_f32_e64 v213, v215, v213
	s_waitcnt lgkmcnt(5)
	v_mfma_f32_32x32x16_bf16 v[98:113], v[124:127], v[130:133], v[98:113]
	v_add_f32_e64 v214, v60, v76
	v_add_f32_e64 v215, v61, v77
	v_add_f32_e64 v126, v62, v78
	v_add_f32_e64 v127, v63, v79
	v_add_f32_e64 v124, v214, v212
	v_add_f32_e64 v125, v215, v213
	v_cvt_pk_bf16_f32 v60, v70, v71
	v_cvt_pk_bf16_f32 v61, v72, v73
	v_cvt_pk_bf16_f32 v62, v74, v75
	v_cvt_pk_bf16_f32 v63, v76, v77
	s_waitcnt lgkmcnt(4)
	v_mfma_f32_32x32x16_bf16 v[82:97], v[224:227], v[130:133], v[82:97]
	v_add_f32_e64 v124, v126, v124
	v_add_f32_e64 v125, v127, v125
	v_add_f32_e64 v126, v64, v80
	v_add_f32_e64 v127, v65, v81
	v_cvt_pk_bf16_f32 v64, v78, v79
	v_cvt_pk_bf16_f32 v65, v80, v81
	ds_read_b64_tr_b16 v[66:67], v202 offset:0
	ds_read_b64_tr_b16 v[68:69], v202 offset:0x400
	ds_read_b64_tr_b16 v[70:71], v202 offset:0x800
	s_waitcnt lgkmcnt(0)
	v_mfma_f32_32x32x16_bf16 v[98:113], v[228:231], v[146:149], v[98:113]
	ds_read_b64_tr_b16 v[72:73], v202 offset:0xc00
	ds_read_b64_tr_b16 v[74:75], v202 offset:0x1000
	ds_read_b64_tr_b16 v[76:77], v202 offset:0x1400
	ds_read_b64_tr_b16 v[78:79], v202 offset:0x1800
	ds_read_b64_tr_b16 v[80:81], v202 offset:0x1c00
	v_add_f32_e64 v124, v126, v124
	v_add_f32_e64 v125, v127, v125
	s_waitcnt lgkmcnt(2)
	v_mfma_f32_32x32x16_bf16 v[82:97], v[232:235], v[146:149], v[82:97]
	v_add_f32_e32 v124, v124, v125
	s_nop 0
	v_mov_b32_e32 v125, v124
	s_nop 1
	v_permlane32_swap_b32_e32 v124, v125
	s_waitcnt lgkmcnt(1)
	v_mfma_f32_32x32x16_bf16 v[98:113], v[208:211], v[142:145], v[98:113]
	ds_read_b64_tr_b16 v[208:209], v202 offset:0x200
	ds_read_b64_tr_b16 v[210:211], v202 offset:0x600
	ds_read_b64_tr_b16 v[212:213], v202 offset:0xa00
	ds_read_b64_tr_b16 v[214:215], v202 offset:0xe00
	ds_read_b64_tr_b16 v[216:217], v202 offset:0x1200
	ds_read_b64_tr_b16 v[218:219], v202 offset:0x1600
	ds_read_b64_tr_b16 v[220:221], v202 offset:0x1a00
	s_waitcnt lgkmcnt(0)
	v_mfma_f32_32x32x16_bf16 v[82:97], v[236:239], v[142:145], v[82:97]
	ds_read_b64_tr_b16 v[222:223], v202 offset:0x1e00
	s_waitcnt lgkmcnt(8)
	v_mfma_f32_32x32x16_bf16 v[18:33], v[50:53], v[66:69], v[18:33]
	s_waitcnt lgkmcnt(0)
	v_mfma_f32_32x32x16_bf16 v[2:17], v[50:53], v[208:211], v[2:17]
	s_nop 8
	v_max_f32_e32 v249, v99, v99
	v_max_f32_e32 v250, v98, v98
	v_max_f32_e32 v249, v250, v249
	v_max3_f32 v249, v249, v100, v101
	v_max3_f32 v249, v249, v102, v103
	v_max3_f32 v251, v249, v104, v105
	v_max3_f32 v251, v251, v106, v107
	v_exp_f32_e32 v50, v98
	v_exp_f32_e32 v51, v99
	v_exp_f32_e32 v52, v100
	v_exp_f32_e32 v53, v101
	v_mov_b64_e32 v[66:67], v[82:83]
	v_mov_b64_e32 v[68:69], v[84:85]
	v_mfma_f32_32x32x16_bf16 v[18:33], v[54:57], v[70:73], v[18:33]
	v_mfma_f32_32x32x16_bf16 v[2:17], v[54:57], v[212:215], v[2:17]
	v_max3_f32 v251, v251, v108, v109
	v_max3_f32 v251, v251, v110, v111
	v_max3_f32 v251, v251, v112, v113
	v_max3_f32 v251, v251, v82, v83
	v_max3_f32 v251, v251, v84, v85
	v_max3_f32 v251, v251, v86, v87
	v_max3_f32 v251, v251, v88, v89
	v_exp_f32_e32 v54, v102
	v_exp_f32_e32 v55, v103
	v_exp_f32_e32 v56, v104
	v_exp_f32_e32 v57, v105
	v_mov_b64_e32 v[70:71], v[86:87]
	v_mov_b64_e32 v[72:73], v[88:89]
	v_mfma_f32_32x32x16_bf16 v[18:33], v[58:61], v[74:77], v[18:33]
	v_mfma_f32_32x32x16_bf16 v[2:17], v[58:61], v[216:219], v[2:17]
	v_max3_f32 v251, v251, v90, v91
	v_max3_f32 v251, v251, v92, v93
	v_max3_f32 v251, v251, v94, v95
	v_max3_f32 v251, v251, v96, v97
	v_mov_b32_e32 v252, v251
	s_nop 1
	v_permlane32_swap_b32_e32 v251, v252
	v_exp_f32_e32 v58, v106
	v_exp_f32_e32 v59, v107
	v_exp_f32_e32 v60, v108
	v_exp_f32_e32 v61, v109
	v_mov_b64_e32 v[74:75], v[90:91]
	v_mov_b64_e32 v[76:77], v[92:93]
	v_mfma_f32_32x32x16_bf16 v[18:33], v[62:65], v[78:81], v[18:33]
	v_mfma_f32_32x32x16_bf16 v[2:17], v[62:65], v[220:223], v[2:17]
	v_exp_f32_e32 v62, v110
	v_exp_f32_e32 v63, v111
	v_exp_f32_e32 v64, v112
	v_exp_f32_e32 v65, v113
	v_mov_b64_e32 v[78:79], v[94:95]
	v_mov_b64_e32 v[80:81], v[96:97]
	v_max_f32_e32 v252, v252, v252
	v_max_f32_e32 v251, v251, v251
	v_max_f32_e32 v126, v251, v252
	v_cmp_ge_f32_e32 vcc, s79, v126
	s_cmp_lg_u64 vcc, exec
	s_cselect_b64 s[6:7], -1, 0
	s_cbranch_scc1 .LBB0_705
	v_mov_b32_e32 v208, 1.0
	v_mov_b32_e32 v209, v203
	s_branch .LBB0_699

; DEVI void attn_unit8(const Params& p, char* smem, int unit, int l, int& cvs  , CvRun& crun) {
;     ...
;         __syncthreads();
;         if (T + 2 < NTILE) B_DMA(T + 2, s2);
.LBB0_702:
	s_mul_i32 s98, s2, 0x6000
	s_add_i32 s98, s96, s98
	s_lshl_b32 s99, s2, 14
	s_add_i32 s99, s97, s99
	s_mul_i32 s6, s61, 0x6000
	s_add_i32 s6, s6, 0
	v_add_u32_e32 v86, s6, v129
	v_lshl_add_u64 v[250:251], v[118:119], 0, s[12:13]
	s_mov_b32 m0, s98
	s_barrier
; template <bool FIRST> DEVI bool partialSM(f32x16& p0, f32x16& p1, float& m_reg, float& alpha) {
;     float pmax = p0[0];
; #pragma unroll
;     for (int r = 1; r < 16; ++r) pmax = fmaxf(pmax, p0[r]);
; #pragma unroll
;     for (int r = 0; r < 16; ++r) pmax = fmaxf(pmax, p1[r]);
;     { auto rr = __builtin_amdgcn_permlane32_swap(__float_as_uint(pmax), __float_as_uint(pmax), false, false);
;       pmax = fmaxf(__uint_as_float(rr[0]), __uint_as_float(rr[1])); }
;     if (FIRST) { m_reg = pmax; alpha = 1.f;
; #pragma unroll
;         for (int r = 0; r < 16; ++r) { p0[r] = __builtin_amdgcn_exp2f(p0[r] - pmax); p1[r] = p1[r] - pmax; }
;         return false;
;     } else if (__builtin_expect(__all(pmax <= ATT_THR), 1)) { alpha = 1.f;
; #pragma unroll
;         for (int r = 0; r < 16; ++r) p0[r] = __builtin_amdgcn_exp2f(p0[r]);
;         return false;
;     } else { const float d = fmaxf(pmax, 0.f); alpha = __builtin_amdgcn_exp2f(-d); m_reg += d;
; #pragma unroll
;         for (int r = 0; r < 16; ++r) { p0[r] = __builtin_amdgcn_exp2f(p0[r] - d); p1[r] = p1[r] - d; }
;         return true;
;     }
; }
; DEVI void finishSM(f32x16& p0, f32x16& p1, float alpha, float& l_reg, bf16x8& pa0, bf16x8& pa1, bf16x8& pa2, bf16x8& pa3) {
; #pragma unroll
;     for (int r = 0; r < 16; ++r) p1[r] = __builtin_amdgcn_exp2f(p1[r]);
;     f32x2 s2 = (f32x2){p0[0], p0[1]} + (f32x2){p1[0], p1[1]};
; #pragma unroll
;     for (int r = 2; r < 16; r += 2) s2 += (f32x2){p0[r], p0[r + 1]} + (f32x2){p1[r], p1[r + 1]};
;     float ps = s2[0] + s2[1];
;     { auto rr = __builtin_amdgcn_permlane32_swap(__float_as_uint(ps), __float_as_uint(ps), false, false);
;       ps = __uint_as_float(rr[0]) + __uint_as_float(rr[1]); }
;     l_reg = l_reg * alpha + ps;
;     ...
;     PK4(p0, 0, pa0); PK4(p0, 8, pa1); PK4(p1, 0, pa2); PK4(p1, 8, pa3);
;     ...
; }
; DEVI void qkt(f32x16& p0, f32x16& p1, const char* Kb, const bf16x8 (&qr)[6], int r32, int hi, const f32x16& cinit) {
; #pragma unroll
;     for (int d0 = 0; d0 < 6; ++d0) { const int cb = (d0 * 16 + hi * 8) * 2;
;         const bf16x8 k0 = *(const bf16x8*)(Kb + KSWZ(r32, cb)), k1 = *(const bf16x8*)(Kb + KSWZ(32 + r32, cb));
;         p0 = __builtin_amdgcn_mfma_f32_32x32x16_bf16(k0, qr[d0], d0 == 0 ? cinit : p0, 0, 0, 0);
;         p1 = __builtin_amdgcn_mfma_f32_32x32x16_bf16(k1, qr[d0], d0 == 0 ? cinit : p1, 0, 0, 0); }
; }
	ds_read_b128 v[82:85], v86
	ds_read_b128 v[210:213], v86 offset:6144
	global_load_lds_dwordx4 v[250:251], off
	v_exp_f32_e32 v66, v66
	s_waitcnt lgkmcnt(0)
	v_mfma_f32_32x32x16_bf16 v[98:113], v[82:85], v[150:153], v[34:49]
	v_add_u32_e32 v126, s6, v184
	v_lshl_add_u64 v[250:251], v[120:121], 0, s[12:13]
	s_add_i32 m0, s98, 0x2000
	v_exp_f32_e32 v67, v67
	v_exp_f32_e32 v68, v68
	global_load_lds_dwordx4 v[250:251], off
	v_exp_f32_e32 v69, v69
	v_exp_f32_e32 v70, v70
	v_exp_f32_e32 v71, v71
	v_exp_f32_e32 v72, v72
	v_mfma_f32_32x32x16_bf16 v[82:97], v[210:213], v[150:153], v[34:49]
	ds_read_b128 v[210:213], v126
	ds_read_b128 v[214:217], v126 offset:6144
	v_add_u32_e32 v126, s6, v185
	v_lshl_add_u64 v[250:251], v[122:123], 0, s[12:13]
	s_add_i32 m0, s98, 0x4000
	v_exp_f32_e32 v73, v73
	v_exp_f32_e32 v74, v74
	global_load_lds_dwordx4 v[250:251], off
	v_exp_f32_e32 v75, v75
	v_exp_f32_e32 v76, v76
	v_exp_f32_e32 v77, v77
	s_waitcnt lgkmcnt(0)
	v_mfma_f32_32x32x16_bf16 v[98:113], v[210:213], v[138:141], v[98:113]
	s_mov_b32 m0, s99
	v_exp_f32_e32 v78, v78
	v_exp_f32_e32 v79, v79
	v_lshl_add_u64 v[250:251], v[116:117], 0, s[40:41]
	global_load_lds_dwordx4 v[116:117], off
	s_add_i32 m0, s99, 0x2000
	v_exp_f32_e32 v80, v80
	v_exp_f32_e32 v81, v81
	v_add_u32_e32 v174, 0x2000, v202
	global_load_lds_dwordx4 v[250:251], off
	v_mfma_f32_32x32x16_bf16 v[82:97], v[214:217], v[138:141], v[82:97]
	ds_read_b128 v[210:213], v126
	ds_read_b128 v[214:217], v126 offset:6144
	v_add_u32_e32 v126, s6, v204
	s_waitcnt lgkmcnt(0)
	v_mfma_f32_32x32x16_bf16 v[98:113], v[210:213], v[134:137], v[98:113]
	ds_read_b128 v[210:213], v126
	ds_read_b128 v[218:221], v126 offset:6144
	v_add_u32_e32 v126, s6, v205
	v_mfma_f32_32x32x16_bf16 v[82:97], v[214:217], v[134:137], v[82:97]
	ds_read_b128 v[214:217], v126
	ds_read_b128 v[222:225], v126 offset:6144
	v_add_u32_e32 v126, s6, v206
	ds_read_b128 v[226:229], v126
	ds_read_b128 v[230:233], v126 offset:6144
	v_add_f32_e32 v126, v50, v66
	v_add_f32_e32 v127, v51, v67
	v_cvt_pk_bf16_f32 v50, v50, v51
	v_cvt_pk_bf16_f32 v51, v52, v53
	s_waitcnt lgkmcnt(0)
	v_mfma_f32_32x32x16_bf16 v[98:113], v[210:213], v[130:133], v[98:113]
	v_add_f32_e64 v210, v52, v68
	v_add_f32_e64 v211, v53, v69
	v_cvt_pk_bf16_f32 v52, v54, v55
	v_cvt_pk_bf16_f32 v53, v56, v57
	v_add_f32_e64 v126, v210, v126
	v_add_f32_e64 v127, v211, v127
	v_add_f32_e64 v210, v54, v70
	v_add_f32_e64 v211, v55, v71
	v_cvt_pk_bf16_f32 v54, v58, v59
	v_mfma_f32_32x32x16_bf16 v[82:97], v[218:221], v[130:133], v[82:97]
	v_add_f32_e64 v126, v210, v126
	v_add_f32_e64 v127, v211, v127
	v_add_f32_e64 v210, v56, v72
	v_add_f32_e64 v211, v57, v73
	v_cvt_pk_bf16_f32 v55, v60, v61
	v_cvt_pk_bf16_f32 v56, v62, v63
	v_cvt_pk_bf16_f32 v57, v64, v65
	v_add_f32_e64 v126, v210, v126
	v_add_f32_e64 v127, v211, v127
	v_add_f32_e32 v210, v58, v74
	v_add_f32_e32 v211, v59, v75
	v_cvt_pk_bf16_f32 v58, v66, v67
	v_cvt_pk_bf16_f32 v59, v68, v69
	v_mfma_f32_32x32x16_bf16 v[98:113], v[214:217], v[146:149], v[98:113]
	v_add_f32_e64 v126, v210, v126
	v_add_f32_e64 v127, v211, v127
	v_add_f32_e64 v210, v60, v76
	v_add_f32_e64 v211, v61, v77
	v_cvt_pk_bf16_f32 v60, v70, v71
	v_cvt_pk_bf16_f32 v61, v72, v73
	v_add_f32_e64 v126, v210, v126
	v_add_f32_e64 v127, v211, v127
	v_add_f32_e32 v210, v62, v78
	v_add_f32_e32 v211, v63, v79
	v_cvt_pk_bf16_f32 v62, v74, v75
	v_cvt_pk_bf16_f32 v63, v76, v77
	v_mfma_f32_32x32x16_bf16 v[82:97], v[222:225], v[146:149], v[82:97]
	v_add_f32_e64 v126, v210, v126
	v_add_f32_e64 v127, v211, v127
	v_add_f32_e64 v210, v64, v80
	v_add_f32_e64 v211, v65, v81
	v_cvt_pk_bf16_f32 v64, v78, v79
	v_cvt_pk_bf16_f32 v65, v80, v81
	ds_read_b64_tr_b16 v[66:67], v174 offset:0
	ds_read_b64_tr_b16 v[68:69], v174 offset:0x400
	ds_read_b64_tr_b16 v[70:71], v174 offset:0x800
	ds_read_b64_tr_b16 v[72:73], v174 offset:0xc00
	ds_read_b64_tr_b16 v[74:75], v174 offset:0x1000
	ds_read_b64_tr_b16 v[76:77], v174 offset:0x1400
	ds_read_b64_tr_b16 v[78:79], v174 offset:0x1800
	ds_read_b64_tr_b16 v[80:81], v174 offset:0x1c00
	v_add_f32_e64 v126, v210, v126
	v_add_f32_e64 v127, v211, v127
	ds_read_b64_tr_b16 v[210:211], v174 offset:0x200
	ds_read_b64_tr_b16 v[212:213], v174 offset:0x600
	ds_read_b64_tr_b16 v[214:215], v174 offset:0xa00
	v_mfma_f32_32x32x16_bf16 v[98:113], v[226:229], v[142:145], v[98:113]
	ds_read_b64_tr_b16 v[216:217], v174 offset:0xe00
	ds_read_b64_tr_b16 v[218:219], v174 offset:0x1200
	ds_read_b64_tr_b16 v[220:221], v174 offset:0x1600
	ds_read_b64_tr_b16 v[222:223], v174 offset:0x1a00
	ds_read_b64_tr_b16 v[224:225], v174 offset:0x1e00
	v_add_f32_e32 v126, v126, v127
	s_waitcnt lgkmcnt(8)
	v_mfma_f32_32x32x16_bf16 v[82:97], v[230:233], v[142:145], v[82:97]
	v_mov_b32_e32 v127, v126
	s_nop 1
	v_permlane32_swap_b32_e32 v126, v127
	v_mfma_f32_32x32x16_bf16 v[18:33], v[50:53], v[66:69], v[18:33]
	s_waitcnt lgkmcnt(0)
	v_mfma_f32_32x32x16_bf16 v[2:17], v[50:53], v[210:213], v[2:17]
	s_nop 4
	v_max_f32_e32 v249, v99, v99
	v_max_f32_e32 v250, v98, v98
	v_max_f32_e32 v249, v250, v249
	v_max3_f32 v249, v249, v100, v101
	v_max3_f32 v249, v249, v102, v103
	v_max3_f32 v251, v249, v104, v105
	v_max3_f32 v251, v251, v106, v107
	v_exp_f32_e32 v50, v98
	v_exp_f32_e32 v51, v99
	v_exp_f32_e32 v52, v100
	v_exp_f32_e32 v53, v101
	v_mov_b64_e32 v[66:67], v[82:83]
	v_mov_b64_e32 v[68:69], v[84:85]
	v_mfma_f32_32x32x16_bf16 v[18:33], v[54:57], v[70:73], v[18:33]
	v_mfma_f32_32x32x16_bf16 v[2:17], v[54:57], v[214:217], v[2:17]
	v_max3_f32 v251, v251, v108, v109
	v_max3_f32 v251, v251, v110, v111
	v_max3_f32 v251, v251, v112, v113
	v_max3_f32 v251, v251, v82, v83
	v_max3_f32 v251, v251, v84, v85
	v_max3_f32 v251, v251, v86, v87
	v_max3_f32 v251, v251, v88, v89
	v_exp_f32_e32 v54, v102
	v_exp_f32_e32 v55, v103
	v_exp_f32_e32 v56, v104
	v_exp_f32_e32 v57, v105
	v_mov_b64_e32 v[70:71], v[86:87]
	v_mov_b64_e32 v[72:73], v[88:89]
	v_mfma_f32_32x32x16_bf16 v[18:33], v[58:61], v[74:77], v[18:33]
	v_mfma_f32_32x32x16_bf16 v[2:17], v[58:61], v[218:221], v[2:17]
	v_max3_f32 v251, v251, v90, v91
	v_max3_f32 v251, v251, v92, v93
	v_max3_f32 v251, v251, v94, v95
	v_max3_f32 v251, v251, v96, v97
	v_mov_b32_e32 v252, v251
	s_nop 1
	v_permlane32_swap_b32_e32 v251, v252
	v_exp_f32_e32 v58, v106
	v_exp_f32_e32 v59, v107
	v_exp_f32_e32 v60, v108
	v_exp_f32_e32 v61, v109
	v_mov_b64_e32 v[74:75], v[90:91]
	v_mov_b64_e32 v[76:77], v[92:93]
	v_mfma_f32_32x32x16_bf16 v[18:33], v[62:65], v[78:81], v[18:33]
	v_mfma_f32_32x32x16_bf16 v[2:17], v[62:65], v[222:225], v[2:17]
	v_exp_f32_e32 v62, v110
	v_exp_f32_e32 v63, v111
	v_exp_f32_e32 v64, v112
	v_exp_f32_e32 v65, v113
	v_mov_b64_e32 v[78:79], v[94:95]
	v_mov_b64_e32 v[80:81], v[96:97]
	v_max_f32_e32 v252, v252, v252
	v_max_f32_e32 v251, v251, v251
	v_max_f32_e32 v174, v251, v252
	v_cmp_ge_f32_e32 vcc, s79, v174
	s_cmp_lg_u64 vcc, exec
	s_cselect_b64 s[6:7], -1, 0
	s_cbranch_scc1 .LBB0_711
	v_mov_b32_e32 v202, 1.0
	v_mov_b32_e32 v203, v209
	s_branch .LBB0_716

; template <bool FIRST> DEVI bool partialSM(f32x16& p0, f32x16& p1, float& m_reg, float& alpha) {
;     float pmax = p0[0];
; #pragma unroll
;     for (int r = 1; r < 16; ++r) pmax = fmaxf(pmax, p0[r]);
; #pragma unroll
;     for (int r = 0; r < 16; ++r) pmax = fmaxf(pmax, p1[r]);
;     { auto rr = __builtin_amdgcn_permlane32_swap(__float_as_uint(pmax), __float_as_uint(pmax), false, false);
;       pmax = fmaxf(__uint_as_float(rr[0]), __uint_as_float(rr[1])); }
;     if (FIRST) { m_reg = pmax; alpha = 1.f;
; #pragma unroll
;         for (int r = 0; r < 16; ++r) { p0[r] = __builtin_amdgcn_exp2f(p0[r] - pmax); p1[r] = p1[r] - pmax; }
;         return false;
;     } else if (__builtin_expect(__all(pmax <= ATT_THR), 1)) { alpha = 1.f;
; #pragma unroll
;         for (int r = 0; r < 16; ++r) p0[r] = __builtin_amdgcn_exp2f(p0[r]);
;         return false;
;     } else { const float d = fmaxf(pmax, 0.f); alpha = __builtin_amdgcn_exp2f(-d); m_reg += d;
; #pragma unroll
;         for (int r = 0; r < 16; ++r) { p0[r] = __builtin_amdgcn_exp2f(p0[r] - d); p1[r] = p1[r] - d; }
;         return true;
;     }
; }
; DEVI void finishSM(f32x16& p0, f32x16& p1, float alpha, float& l_reg, bf16x8& pa0, bf16x8& pa1, bf16x8& pa2, bf16x8& pa3) {
; #pragma unroll
;     for (int r = 0; r < 16; ++r) p1[r] = __builtin_amdgcn_exp2f(p1[r]);
;     f32x2 s2 = (f32x2){p0[0], p0[1]} + (f32x2){p1[0], p1[1]};
; #pragma unroll
;     for (int r = 2; r < 16; r += 2) s2 += (f32x2){p0[r], p0[r + 1]} + (f32x2){p1[r], p1[r + 1]};
;     float ps = s2[0] + s2[1];
;     { auto rr = __builtin_amdgcn_permlane32_swap(__float_as_uint(ps), __float_as_uint(ps), false, false);
;       ps = __uint_as_float(rr[0]) + __uint_as_float(rr[1]); }
;     l_reg = l_reg * alpha + ps;
;     ...
;     PK4(p0, 0, pa0); PK4(p0, 8, pa1); PK4(p1, 0, pa2); PK4(p1, 8, pa3);
;     ...
; }
; DEVI void qkt(f32x16& p0, f32x16& p1, const char* Kb, const bf16x8 (&qr)[6], int r32, int hi, const f32x16& cinit) {
; #pragma unroll
;     for (int d0 = 0; d0 < 6; ++d0) { const int cb = (d0 * 16 + hi * 8) * 2;
;         const bf16x8 k0 = *(const bf16x8*)(Kb + KSWZ(r32, cb)), k1 = *(const bf16x8*)(Kb + KSWZ(32 + r32, cb));
;         p0 = __builtin_amdgcn_mfma_f32_32x32x16_bf16(k0, qr[d0], d0 == 0 ? cinit : p0, 0, 0, 0);
;         p1 = __builtin_amdgcn_mfma_f32_32x32x16_bf16(k1, qr[d0], d0 == 0 ? cinit : p1, 0, 0, 0); }
; }
.LBB0_2260:
	v_add_u32_e32 v174, s98, v205
	v_exp_f32_e32 v66, v66
	v_exp_f32_e32 v67, v67
	s_waitcnt lgkmcnt(0)
	v_mfma_f32_32x32x16_bf16 v[98:113], v[82:85], v[150:153], v[34:49]
	v_add_u32_e32 v82, s98, v184
	v_add_u32_e32 v83, s98, v185
	ds_read_b128 v[210:213], v82 offset:12288
	ds_read_b128 v[214:217], v82 offset:18432
	ds_read_b128 v[218:221], v83 offset:12288
	ds_read_b128 v[222:225], v83 offset:18432
	v_exp_f32_e32 v68, v68
	v_exp_f32_e32 v69, v69
	v_exp_f32_e32 v70, v70
	v_exp_f32_e32 v71, v71
	s_waitcnt lgkmcnt(4)
	v_mfma_f32_32x32x16_bf16 v[82:97], v[124:127], v[150:153], v[34:49]
	ds_read_b128 v[124:127], v174 offset:12288
	ds_read_b128 v[226:229], v174 offset:18432
	v_exp_f32_e32 v72, v72
	v_exp_f32_e32 v73, v73
	v_exp_f32_e32 v74, v74
	v_exp_f32_e32 v75, v75
	v_exp_f32_e32 v76, v76
	v_exp_f32_e32 v77, v77
	s_waitcnt lgkmcnt(0)
	v_mfma_f32_32x32x16_bf16 v[98:113], v[210:213], v[138:141], v[98:113]
	v_add_u32_e32 v174, s98, v206
	v_exp_f32_e32 v78, v78
	v_exp_f32_e32 v79, v79
	ds_read_b128 v[230:233], v174 offset:12288
	ds_read_b128 v[234:237], v174 offset:18432
	v_exp_f32_e32 v80, v80
	v_exp_f32_e32 v81, v81
	v_add_u32_e32 v174, s98, v207
	s_waitcnt lgkmcnt(6)
	v_mfma_f32_32x32x16_bf16 v[82:97], v[214:217], v[138:141], v[82:97]
	v_add_f32_e64 v214, v50, v66
	v_add_f32_e64 v215, v51, v67
	v_add_f32_e64 v216, v52, v68
	v_add_f32_e64 v217, v53, v69
	v_lshl_add_u32 v203, s71, 14, v115
	v_add_f32_e32 v214, v216, v214
	v_add_f32_e32 v215, v217, v215
	v_add_f32_e32 v216, v54, v70
	v_add_f32_e32 v217, v55, v71
	ds_read_b128 v[210:213], v174 offset:12288
	ds_read_b128 v[238:241], v174 offset:18432
	v_add_f32_e32 v214, v216, v214
	v_add_f32_e32 v215, v217, v215
	s_waitcnt lgkmcnt(7)
	v_mfma_f32_32x32x16_bf16 v[98:113], v[218:221], v[134:137], v[98:113]
	v_add_f32_e64 v216, v56, v72
	v_add_f32_e64 v217, v57, v73
	v_cvt_pk_bf16_f32 v50, v50, v51
	v_cvt_pk_bf16_f32 v51, v52, v53
	v_cvt_pk_bf16_f32 v52, v54, v55
	v_cvt_pk_bf16_f32 v53, v56, v57
	v_cvt_pk_bf16_f32 v54, v58, v59
	v_add_f32_e64 v214, v216, v214
	v_add_f32_e64 v215, v217, v215
	s_waitcnt lgkmcnt(6)
	v_mfma_f32_32x32x16_bf16 v[82:97], v[222:225], v[134:137], v[82:97]
	v_add_f32_e64 v216, v58, v74
	v_add_f32_e64 v217, v59, v75
	v_cvt_pk_bf16_f32 v55, v60, v61
	v_cvt_pk_bf16_f32 v56, v62, v63
	v_cvt_pk_bf16_f32 v57, v64, v65
	v_cvt_pk_bf16_f32 v58, v66, v67
	v_cvt_pk_bf16_f32 v59, v68, v69
	v_add_f32_e64 v214, v216, v214
	v_add_f32_e64 v215, v217, v215
	s_waitcnt lgkmcnt(5)
	v_mfma_f32_32x32x16_bf16 v[98:113], v[124:127], v[130:133], v[98:113]
	v_add_f32_e64 v216, v60, v76
	v_add_f32_e64 v217, v61, v77
	v_add_f32_e64 v126, v62, v78
	v_add_f32_e64 v127, v63, v79
	v_add_f32_e64 v124, v216, v214
	v_add_f32_e64 v125, v217, v215
	v_cvt_pk_bf16_f32 v60, v70, v71
	v_cvt_pk_bf16_f32 v61, v72, v73
	v_cvt_pk_bf16_f32 v62, v74, v75
	v_cvt_pk_bf16_f32 v63, v76, v77
	s_waitcnt lgkmcnt(4)
	v_mfma_f32_32x32x16_bf16 v[82:97], v[226:229], v[130:133], v[82:97]
	v_add_f32_e64 v124, v126, v124
	v_add_f32_e64 v125, v127, v125
	v_add_f32_e64 v126, v64, v80
	v_add_f32_e64 v127, v65, v81
	v_cvt_pk_bf16_f32 v64, v78, v79
	v_cvt_pk_bf16_f32 v65, v80, v81
	ds_read_b64_tr_b16 v[66:67], v203 offset:0
	ds_read_b64_tr_b16 v[68:69], v203 offset:0x400
	ds_read_b64_tr_b16 v[70:71], v203 offset:0x800
	s_waitcnt lgkmcnt(0)
	v_mfma_f32_32x32x16_bf16 v[98:113], v[230:233], v[146:149], v[98:113]
	ds_read_b64_tr_b16 v[72:73], v203 offset:0xc00
	ds_read_b64_tr_b16 v[74:75], v203 offset:0x1000
	ds_read_b64_tr_b16 v[76:77], v203 offset:0x1400
	ds_read_b64_tr_b16 v[78:79], v203 offset:0x1800
	ds_read_b64_tr_b16 v[80:81], v203 offset:0x1c00
	v_add_f32_e64 v124, v126, v124
	v_add_f32_e64 v125, v127, v125
	s_waitcnt lgkmcnt(2)
	v_mfma_f32_32x32x16_bf16 v[82:97], v[234:237], v[146:149], v[82:97]
	v_add_f32_e32 v124, v124, v125
	s_nop 0
	v_mov_b32_e32 v125, v124
	s_nop 1
	v_permlane32_swap_b32_e32 v124, v125
	s_waitcnt lgkmcnt(1)
	v_mfma_f32_32x32x16_bf16 v[98:113], v[210:213], v[142:145], v[98:113]
	ds_read_b64_tr_b16 v[210:211], v203 offset:0x200
	ds_read_b64_tr_b16 v[212:213], v203 offset:0x600
	ds_read_b64_tr_b16 v[214:215], v203 offset:0xa00
	ds_read_b64_tr_b16 v[216:217], v203 offset:0xe00
	ds_read_b64_tr_b16 v[218:219], v203 offset:0x1200
	ds_read_b64_tr_b16 v[220:221], v203 offset:0x1600
	ds_read_b64_tr_b16 v[222:223], v203 offset:0x1a00
	s_waitcnt lgkmcnt(0)
	v_mfma_f32_32x32x16_bf16 v[82:97], v[238:241], v[142:145], v[82:97]
	ds_read_b64_tr_b16 v[224:225], v203 offset:0x1e00
	s_waitcnt lgkmcnt(8)
	v_mfma_f32_32x32x16_bf16 v[18:33], v[50:53], v[66:69], v[18:33]
	s_waitcnt lgkmcnt(0)
	v_mfma_f32_32x32x16_bf16 v[2:17], v[50:53], v[210:213], v[2:17]
	s_nop 8
	v_max_f32_e32 v249, v99, v99
	v_max_f32_e32 v250, v98, v98
	v_max_f32_e32 v249, v250, v249
	v_max3_f32 v249, v249, v100, v101
	v_max3_f32 v249, v249, v102, v103
	v_max3_f32 v251, v249, v104, v105
	v_max3_f32 v251, v251, v106, v107
	v_exp_f32_e32 v50, v98
	v_exp_f32_e32 v51, v99
	v_exp_f32_e32 v52, v100
	v_exp_f32_e32 v53, v101
	v_mov_b64_e32 v[66:67], v[82:83]
	v_mov_b64_e32 v[68:69], v[84:85]
	v_mfma_f32_32x32x16_bf16 v[18:33], v[54:57], v[70:73], v[18:33]
	v_mfma_f32_32x32x16_bf16 v[2:17], v[54:57], v[214:217], v[2:17]
	v_max3_f32 v251, v251, v108, v109
	v_max3_f32 v251, v251, v110, v111
	v_max3_f32 v251, v251, v112, v113
	v_max3_f32 v251, v251, v82, v83
	v_max3_f32 v251, v251, v84, v85
	v_max3_f32 v251, v251, v86, v87
	v_max3_f32 v251, v251, v88, v89
	v_exp_f32_e32 v54, v102
	v_exp_f32_e32 v55, v103
	v_exp_f32_e32 v56, v104
	v_exp_f32_e32 v57, v105
	v_mov_b64_e32 v[70:71], v[86:87]
	v_mov_b64_e32 v[72:73], v[88:89]
	v_mfma_f32_32x32x16_bf16 v[18:33], v[58:61], v[74:77], v[18:33]
	v_mfma_f32_32x32x16_bf16 v[2:17], v[58:61], v[218:221], v[2:17]
	v_max3_f32 v251, v251, v90, v91
	v_max3_f32 v251, v251, v92, v93
	v_max3_f32 v251, v251, v94, v95
	v_max3_f32 v251, v251, v96, v97
	v_mov_b32_e32 v252, v251
	s_nop 1
	v_permlane32_swap_b32_e32 v251, v252
	v_exp_f32_e32 v58, v106
	v_exp_f32_e32 v59, v107
	v_exp_f32_e32 v60, v108
	v_exp_f32_e32 v61, v109
	v_mov_b64_e32 v[74:75], v[90:91]
	v_mov_b64_e32 v[76:77], v[92:93]
	v_mfma_f32_32x32x16_bf16 v[18:33], v[62:65], v[78:81], v[18:33]
	v_mfma_f32_32x32x16_bf16 v[2:17], v[62:65], v[222:225], v[2:17]
	v_exp_f32_e32 v62, v110
	v_exp_f32_e32 v63, v111
	v_exp_f32_e32 v64, v112
	v_exp_f32_e32 v65, v113
	v_mov_b64_e32 v[78:79], v[94:95]
	v_mov_b64_e32 v[80:81], v[96:97]
	v_max_f32_e32 v252, v252, v252
	v_max_f32_e32 v251, v251, v251
	v_max_f32_e32 v126, v251, v252
	v_cmp_ge_f32_e32 vcc, s80, v126
	s_cmp_lg_u64 vcc, exec
	s_cselect_b64 s[6:7], -1, 0
	s_cbranch_scc1 .LBB0_2269
	v_mov_b32_e32 v209, 1.0
	v_mov_b32_e32 v210, v204
	s_branch .LBB0_2263

; #define VM0() asm volatile("s_waitcnt vmcnt(0)" ::: "memory")
; DEVI void attn_unit8(const Params& p, char* smem, int unit, int l, int& cvs  , CvRun& crun) {
;     ...
;         if (cvr.live) asm volatile("s_waitcnt vmcnt(2)" ::: "memory"); else VM0();
;         __syncthreads();
;         if (T + 2 < NTILE) B_DMA(T + 2, s2);
;         qkt(pA0, pA1, K_lds + s1 * 24576, qr, r32, hi, cinit);
.LBB0_2266:
	s_mul_i32 s98, s61, 0x6000
	s_add_i32 s98, s96, s98
	s_lshl_b32 s99, s61, 14
	s_add_i32 s99, s97, s99
	s_mul_i32 s6, s2, 0x6000
	s_add_i32 s6, s6, 0
	v_add_u32_e32 v86, s6, v129
	v_lshl_add_u64 v[250:251], v[118:119], 0, s[12:13]
	s_mov_b32 m0, s98
	s_barrier
; template <bool FIRST> DEVI bool partialSM(f32x16& p0, f32x16& p1, float& m_reg, float& alpha) {
;     float pmax = p0[0];
; #pragma unroll
;     for (int r = 1; r < 16; ++r) pmax = fmaxf(pmax, p0[r]);
; #pragma unroll
;     for (int r = 0; r < 16; ++r) pmax = fmaxf(pmax, p1[r]);
;     { auto rr = __builtin_amdgcn_permlane32_swap(__float_as_uint(pmax), __float_as_uint(pmax), false, false);
;       pmax = fmaxf(__uint_as_float(rr[0]), __uint_as_float(rr[1])); }
;     if (FIRST) { m_reg = pmax; alpha = 1.f;
; #pragma unroll
;         for (int r = 0; r < 16; ++r) { p0[r] = __builtin_amdgcn_exp2f(p0[r] - pmax); p1[r] = p1[r] - pmax; }
;         return false;
;     } else if (__builtin_expect(__all(pmax <= ATT_THR), 1)) { alpha = 1.f;
; #pragma unroll
;         for (int r = 0; r < 16; ++r) p0[r] = __builtin_amdgcn_exp2f(p0[r]);
;         return false;
;     } else { const float d = fmaxf(pmax, 0.f); alpha = __builtin_amdgcn_exp2f(-d); m_reg += d;
; #pragma unroll
;         for (int r = 0; r < 16; ++r) { p0[r] = __builtin_amdgcn_exp2f(p0[r] - d); p1[r] = p1[r] - d; }
;         return true;
;     }
; }
; DEVI void finishSM(f32x16& p0, f32x16& p1, float alpha, float& l_reg, bf16x8& pa0, bf16x8& pa1, bf16x8& pa2, bf16x8& pa3) {
; #pragma unroll
;     for (int r = 0; r < 16; ++r) p1[r] = __builtin_amdgcn_exp2f(p1[r]);
;     f32x2 s2 = (f32x2){p0[0], p0[1]} + (f32x2){p1[0], p1[1]};
; #pragma unroll
;     for (int r = 2; r < 16; r += 2) s2 += (f32x2){p0[r], p0[r + 1]} + (f32x2){p1[r], p1[r + 1]};
;     float ps = s2[0] + s2[1];
;     { auto rr = __builtin_amdgcn_permlane32_swap(__float_as_uint(ps), __float_as_uint(ps), false, false);
;       ps = __uint_as_float(rr[0]) + __uint_as_float(rr[1]); }
;     l_reg = l_reg * alpha + ps;
;     ...
;     PK4(p0, 0, pa0); PK4(p0, 8, pa1); PK4(p1, 0, pa2); PK4(p1, 8, pa3);
;     ...
; }
; DEVI void qkt(f32x16& p0, f32x16& p1, const char* Kb, const bf16x8 (&qr)[6], int r32, int hi, const f32x16& cinit) {
; #pragma unroll
;     for (int d0 = 0; d0 < 6; ++d0) { const int cb = (d0 * 16 + hi * 8) * 2;
;         const bf16x8 k0 = *(const bf16x8*)(Kb + KSWZ(r32, cb)), k1 = *(const bf16x8*)(Kb + KSWZ(32 + r32, cb));
;         p0 = __builtin_amdgcn_mfma_f32_32x32x16_bf16(k0, qr[d0], d0 == 0 ? cinit : p0, 0, 0, 0);
;         p1 = __builtin_amdgcn_mfma_f32_32x32x16_bf16(k1, qr[d0], d0 == 0 ? cinit : p1, 0, 0, 0); }
; }
	ds_read_b128 v[82:85], v86
	ds_read_b128 v[212:215], v86 offset:6144
	global_load_lds_dwordx4 v[250:251], off
	v_exp_f32_e32 v66, v66
	s_waitcnt lgkmcnt(0)
	v_mfma_f32_32x32x16_bf16 v[98:113], v[82:85], v[150:153], v[34:49]
	v_add_u32_e32 v126, s6, v184
	v_lshl_add_u64 v[250:251], v[120:121], 0, s[12:13]
	s_add_i32 m0, s98, 0x2000
	v_exp_f32_e32 v67, v67
	v_exp_f32_e32 v68, v68
	global_load_lds_dwordx4 v[250:251], off
	v_exp_f32_e32 v69, v69
	v_exp_f32_e32 v70, v70
	v_exp_f32_e32 v71, v71
	v_exp_f32_e32 v72, v72
	v_mfma_f32_32x32x16_bf16 v[82:97], v[212:215], v[150:153], v[34:49]
	ds_read_b128 v[212:215], v126
	ds_read_b128 v[216:219], v126 offset:6144
	v_add_u32_e32 v126, s6, v185
	v_lshl_add_u64 v[250:251], v[122:123], 0, s[12:13]
	s_add_i32 m0, s98, 0x4000
	v_exp_f32_e32 v73, v73
	v_exp_f32_e32 v74, v74
	global_load_lds_dwordx4 v[250:251], off
	v_exp_f32_e32 v75, v75
	v_exp_f32_e32 v76, v76
	v_exp_f32_e32 v77, v77
	s_waitcnt lgkmcnt(0)
	v_mfma_f32_32x32x16_bf16 v[98:113], v[212:215], v[138:141], v[98:113]
	s_mov_b32 m0, s99
	v_exp_f32_e32 v78, v78
	v_exp_f32_e32 v79, v79
	v_lshl_add_u64 v[250:251], v[116:117], 0, s[40:41]
	global_load_lds_dwordx4 v[116:117], off
	s_add_i32 m0, s99, 0x2000
	v_exp_f32_e32 v80, v80
	v_exp_f32_e32 v81, v81
	v_add_u32_e32 v174, 0x2000, v203
	global_load_lds_dwordx4 v[250:251], off
	v_mfma_f32_32x32x16_bf16 v[82:97], v[216:219], v[138:141], v[82:97]
	ds_read_b128 v[212:215], v126
	ds_read_b128 v[216:219], v126 offset:6144
	v_add_u32_e32 v126, s6, v205
	s_waitcnt lgkmcnt(0)
	v_mfma_f32_32x32x16_bf16 v[98:113], v[212:215], v[134:137], v[98:113]
	ds_read_b128 v[212:215], v126
	ds_read_b128 v[220:223], v126 offset:6144
	v_add_u32_e32 v126, s6, v206
	v_mfma_f32_32x32x16_bf16 v[82:97], v[216:219], v[134:137], v[82:97]
	ds_read_b128 v[216:219], v126
	ds_read_b128 v[224:227], v126 offset:6144
	v_add_u32_e32 v126, s6, v207
	ds_read_b128 v[228:231], v126
	ds_read_b128 v[232:235], v126 offset:6144
	v_add_f32_e32 v126, v50, v66
	v_add_f32_e32 v127, v51, v67
	v_cvt_pk_bf16_f32 v50, v50, v51
	v_cvt_pk_bf16_f32 v51, v52, v53
	s_waitcnt lgkmcnt(0)
	v_mfma_f32_32x32x16_bf16 v[98:113], v[212:215], v[130:133], v[98:113]
	v_add_f32_e64 v212, v52, v68
	v_add_f32_e64 v213, v53, v69
	v_cvt_pk_bf16_f32 v52, v54, v55
	v_cvt_pk_bf16_f32 v53, v56, v57
	v_add_f32_e64 v126, v212, v126
	v_add_f32_e64 v127, v213, v127
	v_add_f32_e64 v212, v54, v70
	v_add_f32_e64 v213, v55, v71
	v_cvt_pk_bf16_f32 v54, v58, v59
	v_mfma_f32_32x32x16_bf16 v[82:97], v[220:223], v[130:133], v[82:97]
	v_add_f32_e64 v126, v212, v126
	v_add_f32_e64 v127, v213, v127
	v_add_f32_e64 v212, v56, v72
	v_add_f32_e64 v213, v57, v73
	v_cvt_pk_bf16_f32 v55, v60, v61
	v_cvt_pk_bf16_f32 v56, v62, v63
	v_cvt_pk_bf16_f32 v57, v64, v65
	v_add_f32_e64 v126, v212, v126
	v_add_f32_e64 v127, v213, v127
	v_add_f32_e32 v212, v58, v74
	v_add_f32_e32 v213, v59, v75
	v_cvt_pk_bf16_f32 v58, v66, v67
	v_cvt_pk_bf16_f32 v59, v68, v69
	v_mfma_f32_32x32x16_bf16 v[98:113], v[216:219], v[146:149], v[98:113]
	v_add_f32_e64 v126, v212, v126
	v_add_f32_e64 v127, v213, v127
	v_add_f32_e64 v212, v60, v76
	v_add_f32_e64 v213, v61, v77
	v_cvt_pk_bf16_f32 v60, v70, v71
	v_cvt_pk_bf16_f32 v61, v72, v73
	v_add_f32_e64 v126, v212, v126
	v_add_f32_e64 v127, v213, v127
	v_add_f32_e32 v212, v62, v78
	v_add_f32_e32 v213, v63, v79
	v_cvt_pk_bf16_f32 v62, v74, v75
	v_cvt_pk_bf16_f32 v63, v76, v77
	v_mfma_f32_32x32x16_bf16 v[82:97], v[224:227], v[146:149], v[82:97]
	v_add_f32_e64 v126, v212, v126
	v_add_f32_e64 v127, v213, v127
	v_add_f32_e64 v212, v64, v80
	v_add_f32_e64 v213, v65, v81
	v_cvt_pk_bf16_f32 v64, v78, v79
	v_cvt_pk_bf16_f32 v65, v80, v81
	ds_read_b64_tr_b16 v[66:67], v174 offset:0
	ds_read_b64_tr_b16 v[68:69], v174 offset:0x400
	ds_read_b64_tr_b16 v[70:71], v174 offset:0x800
	ds_read_b64_tr_b16 v[72:73], v174 offset:0xc00
	ds_read_b64_tr_b16 v[74:75], v174 offset:0x1000
	ds_read_b64_tr_b16 v[76:77], v174 offset:0x1400
	ds_read_b64_tr_b16 v[78:79], v174 offset:0x1800
	ds_read_b64_tr_b16 v[80:81], v174 offset:0x1c00
	v_add_f32_e64 v126, v212, v126
	v_add_f32_e64 v127, v213, v127
	ds_read_b64_tr_b16 v[212:213], v174 offset:0x200
	ds_read_b64_tr_b16 v[214:215], v174 offset:0x600
	ds_read_b64_tr_b16 v[216:217], v174 offset:0xa00
	v_mfma_f32_32x32x16_bf16 v[98:113], v[228:231], v[142:145], v[98:113]
	ds_read_b64_tr_b16 v[218:219], v174 offset:0xe00
	ds_read_b64_tr_b16 v[220:221], v174 offset:0x1200
	ds_read_b64_tr_b16 v[222:223], v174 offset:0x1600
	ds_read_b64_tr_b16 v[224:225], v174 offset:0x1a00
	ds_read_b64_tr_b16 v[226:227], v174 offset:0x1e00
	v_add_f32_e32 v126, v126, v127
	s_waitcnt lgkmcnt(8)
	v_mfma_f32_32x32x16_bf16 v[82:97], v[232:235], v[142:145], v[82:97]
	v_mov_b32_e32 v127, v126
	s_nop 1
	v_permlane32_swap_b32_e32 v126, v127
	v_mfma_f32_32x32x16_bf16 v[18:33], v[50:53], v[66:69], v[18:33]
	s_waitcnt lgkmcnt(0)
	v_mfma_f32_32x32x16_bf16 v[2:17], v[50:53], v[212:215], v[2:17]
	s_nop 4
	v_max_f32_e32 v249, v99, v99
	v_max_f32_e32 v250, v98, v98
	v_max_f32_e32 v249, v250, v249
	v_max3_f32 v249, v249, v100, v101
	v_max3_f32 v249, v249, v102, v103
	v_max3_f32 v251, v249, v104, v105
	v_max3_f32 v251, v251, v106, v107
	v_exp_f32_e32 v50, v98
	v_exp_f32_e32 v51, v99
	v_exp_f32_e32 v52, v100
	v_exp_f32_e32 v53, v101
	v_mov_b64_e32 v[66:67], v[82:83]
	v_mov_b64_e32 v[68:69], v[84:85]
	v_mfma_f32_32x32x16_bf16 v[18:33], v[54:57], v[70:73], v[18:33]
	v_mfma_f32_32x32x16_bf16 v[2:17], v[54:57], v[216:219], v[2:17]
	v_max3_f32 v251, v251, v108, v109
	v_max3_f32 v251, v251, v110, v111
	v_max3_f32 v251, v251, v112, v113
	v_max3_f32 v251, v251, v82, v83
	v_max3_f32 v251, v251, v84, v85
	v_max3_f32 v251, v251, v86, v87
	v_max3_f32 v251, v251, v88, v89
	v_exp_f32_e32 v54, v102
	v_exp_f32_e32 v55, v103
	v_exp_f32_e32 v56, v104
	v_exp_f32_e32 v57, v105
	v_mov_b64_e32 v[70:71], v[86:87]
	v_mov_b64_e32 v[72:73], v[88:89]
	v_mfma_f32_32x32x16_bf16 v[18:33], v[58:61], v[74:77], v[18:33]
	v_mfma_f32_32x32x16_bf16 v[2:17], v[58:61], v[220:223], v[2:17]
	v_max3_f32 v251, v251, v90, v91
	v_max3_f32 v251, v251, v92, v93
	v_max3_f32 v251, v251, v94, v95
	v_max3_f32 v251, v251, v96, v97
	v_mov_b32_e32 v252, v251
	s_nop 1
	v_permlane32_swap_b32_e32 v251, v252
	v_exp_f32_e32 v58, v106
	v_exp_f32_e32 v59, v107
	v_exp_f32_e32 v60, v108
	v_exp_f32_e32 v61, v109
	v_mov_b64_e32 v[74:75], v[90:91]
	v_mov_b64_e32 v[76:77], v[92:93]
	v_mfma_f32_32x32x16_bf16 v[18:33], v[62:65], v[78:81], v[18:33]
	v_mfma_f32_32x32x16_bf16 v[2:17], v[62:65], v[224:227], v[2:17]
	v_exp_f32_e32 v62, v110
	v_exp_f32_e32 v63, v111
	v_exp_f32_e32 v64, v112
	v_exp_f32_e32 v65, v113
	v_mov_b64_e32 v[78:79], v[94:95]
	v_mov_b64_e32 v[80:81], v[96:97]
	v_max_f32_e32 v252, v252, v252
	v_max_f32_e32 v251, v251, v251
	v_max_f32_e32 v174, v251, v252
	v_cmp_ge_f32_e32 vcc, s80, v174
	s_cmp_lg_u64 vcc, exec
	s_cselect_b64 s[6:7], -1, 0
	s_cbranch_scc1 .LBB0_2275
	v_mov_b32_e32 v203, 1.0
	v_mov_b32_e32 v204, v210
	s_branch .LBB0_2280
